# MLA up-projection RoPE tile epilogue: cos/sin rows, k_rope pieces and the q/k rope stores go through a lane re-ordering (four consecutive lanes = one row's contiguous bytes) with ds_bpermute
# speedup vs baseline: 1.0053x; 1.0053x over previous
; __device__ __forceinline__ unsigned cvt_pk_bf16(float lo, float hi) { f32x2 v = {lo, hi}; bf16x2_t b = __builtin_convertvector(v, bf16x2_t); return __builtin_bit_cast(unsigned, b); }
;     __device__ __forceinline__ void operator()(const f32x4 (&acc)[2][2][4][2], const u32x2 (&pf)[8], const g8::Unit& u, int wr, int wc, int fr, int fq) const {
;     ...
;                 if (u.pn == 1) {
;                     const float rq = __builtin_amdgcn_rsqf(sq.x * (1.f / 256.f) + 1e-6f) * SCALE_A;
;                     const float* cp = cs + ((size_t)(row % S) * 16 + 4 * fq) * 2;
;                     const f32x4 c0 = *(const f32x4*)cp, c1 = *(const f32x4*)(cp + 4);
;                     const float cc[4] = {c0[0], c0[2], c1[0], c1[2]}, sn[4] = {c0[1], c0[3], c1[1], c1[3]};
;                     {   const f32x4 t1 = acc[ai][0][m][0] * rq, t2 = acc[ai][0][m][1] * rq;
;                         float o1[4], o2[4];
; #pragma unroll
;                         for (int j = 0; j < 4; ++j) { o1[j] = t1[j] * cc[j] - t2[j] * sn[j]; o2[j] = t1[j] * sn[j] + t2[j] * cc[j]; }
;                         bf16_t* qp = QA + (size_t)row * 384 + wc * 96 + 64 + 4 * fq;
;                         *(u32x2*)qp = (u32x2){cvt_pk_bf16(o1[0], o1[1]), cvt_pk_bf16(o1[2], o1[3])};
;                         *(u32x2*)(qp + 16) = (u32x2){cvt_pk_bf16(o2[0], o2[1]), cvt_pk_bf16(o2[2], o2[3])}; }
;                     {   const bf16_t* hp = H + (size_t)row * HP + C_KR + 4 * fq;
;                         const u32x2 a = *(const u32x2*)hp, b = *(const u32x2*)(hp + 16);
.LBB0_563:
	s_cmp_eq_u32 s67, 1
	s_mov_b64 s[14:15], -1
	s_cbranch_scc0 .LBB0_565
	v_mbcnt_lo_u32_b32 v4, -1, 0
	v_mbcnt_hi_u32_b32 v4, -1, v4
	v_and_b32_e32 v143, 3, v4
	v_lshrrev_b32_e32 v142, 2, v4
	v_and_b32_e32 v140, 15, v4
	v_sub_u32_e32 v142, v142, v140
	v_lshlrev_b32_e32 v141, 4, v140
	v_lshrrev_b32_e32 v140, 4, v4
	v_lshl_or_b32 v141, v140, 2, v141
	v_sub_u32_e32 v156, v143, v140
	v_lshlrev_b32_e32 v156, 3, v156
	v_ashrrev_i32_e32 v157, 31, v156
	v_mad_i64_i32 v[144:145], s[14:15], v142, s0, v[156:157]
	v_and_b32_e32 v140, 60, v4
	v_lshl_or_b32 v140, v143, 6, v140
	v_lshlrev_b32_e32 v198, 3, v143
	v_mov_b32_e32 v199, v31
	v_add_u32_e32 v4, v142, v164
	v_ashrrev_i32_e32 v196, 31, v4
	v_lshrrev_b32_e32 v196, 19, v196
	v_add_u32_e32 v196, v4, v196
	v_and_b32_e32 v196, 0xffffe000, v196
	v_sub_u32_e32 v196, v4, v196
	v_ashrrev_i32_e32 v197, 31, v196
	v_lshlrev_b64 v[196:197], 7, v[196:197]
	v_lshl_add_u64 v[196:197], s[46:47], 0, v[196:197]
	v_lshl_add_u64 v[196:197], v[198:199], 2, v[196:197]
	global_load_dwordx4 v[206:209], v[196:197], off offset:16
	global_load_dwordx4 v[210:213], v[196:197], off
	v_mov_b64_e32 v[196:197], s[44:45]
	v_mad_i64_i32 v[196:197], s[14:15], v4, s33, v[196:197]
	v_lshl_add_u64 v[196:197], v[196:197], 0, v[198:199]
	global_load_dwordx2 v[214:215], v[196:197], off offset:768
	global_load_dwordx2 v[216:217], v[196:197], off offset:800
	v_add_u32_e32 v4, 0x10, v164
	v_add_u32_e32 v4, v142, v4
	v_ashrrev_i32_e32 v196, 31, v4
	v_lshrrev_b32_e32 v196, 19, v196
	v_add_u32_e32 v196, v4, v196
	v_and_b32_e32 v196, 0xffffe000, v196
	v_sub_u32_e32 v196, v4, v196
	v_ashrrev_i32_e32 v197, 31, v196
	v_lshlrev_b64 v[196:197], 7, v[196:197]
	v_lshl_add_u64 v[196:197], s[46:47], 0, v[196:197]
	v_lshl_add_u64 v[196:197], v[198:199], 2, v[196:197]
	global_load_dwordx4 v[218:221], v[196:197], off offset:16
	global_load_dwordx4 v[222:225], v[196:197], off
	v_mov_b64_e32 v[196:197], s[44:45]
	v_mad_i64_i32 v[196:197], s[14:15], v4, s33, v[196:197]
	v_lshl_add_u64 v[196:197], v[196:197], 0, v[198:199]
	global_load_dwordx2 v[226:227], v[196:197], off offset:768
	global_load_dwordx2 v[228:229], v[196:197], off offset:800
	v_add_u32_e32 v4, 0x20, v164
	v_add_u32_e32 v4, v142, v4
	v_ashrrev_i32_e32 v196, 31, v4
	v_lshrrev_b32_e32 v196, 19, v196
	v_add_u32_e32 v196, v4, v196
	v_and_b32_e32 v196, 0xffffe000, v196
	v_sub_u32_e32 v196, v4, v196
	v_ashrrev_i32_e32 v197, 31, v196
	v_lshlrev_b64 v[196:197], 7, v[196:197]
	v_lshl_add_u64 v[196:197], s[46:47], 0, v[196:197]
	v_lshl_add_u64 v[196:197], v[198:199], 2, v[196:197]
	global_load_dwordx4 v[230:233], v[196:197], off offset:16
	global_load_dwordx4 v[234:237], v[196:197], off
	v_mov_b64_e32 v[196:197], s[44:45]
	v_mad_i64_i32 v[196:197], s[14:15], v4, s33, v[196:197]
	v_lshl_add_u64 v[196:197], v[196:197], 0, v[198:199]
	global_load_dwordx2 v[238:239], v[196:197], off offset:768
	global_load_dwordx2 v[240:241], v[196:197], off offset:800
	v_add_u32_e32 v4, 0x30, v164
	v_add_u32_e32 v4, v142, v4
	v_ashrrev_i32_e32 v196, 31, v4
	v_lshrrev_b32_e32 v196, 19, v196
	v_add_u32_e32 v196, v4, v196
	v_and_b32_e32 v196, 0xffffe000, v196
	v_sub_u32_e32 v196, v4, v196
	v_ashrrev_i32_e32 v197, 31, v196
	v_lshlrev_b64 v[196:197], 7, v[196:197]
	v_lshl_add_u64 v[196:197], s[46:47], 0, v[196:197]
	v_lshl_add_u64 v[196:197], v[198:199], 2, v[196:197]
	global_load_dwordx4 v[242:245], v[196:197], off offset:16
	global_load_dwordx4 v[188:191], v[196:197], off
	v_mov_b64_e32 v[196:197], s[44:45]
	v_mad_i64_i32 v[196:197], s[14:15], v4, s33, v[196:197]
	v_lshl_add_u64 v[196:197], v[196:197], 0, v[198:199]
	global_load_dwordx2 v[192:193], v[196:197], off offset:768
	global_load_dwordx2 v[194:195], v[196:197], off offset:800
	v_fmamk_f32 v132, v176, 0x3b800000, v246
	v_rsq_f32_e32 v132, v132
	v_lshlrev_b32_e32 v186, 1, v5
	v_mov_b32_e32 v187, v31
	v_mul_f32_e32 v150, 0x3e16c740, v132
	v_ashrrev_i32_e32 v132, 31, v164
	v_lshrrev_b32_e32 v132, 19, v132
	v_add_u32_e32 v132, v164, v132
	v_and_b32_e32 v132, 0xffffe000, v132
	v_sub_u32_e32 v132, v164, v132
	v_ashrrev_i32_e32 v133, 31, v132
	v_lshlrev_b64 v[132:133], 7, v[132:133]
	v_lshl_add_u64 v[132:133], s[46:47], 0, v[132:133]
	v_lshl_add_u64 v[136:137], v[132:133], 0, v[30:31]
	s_waitcnt vmcnt(12)
; __device__ __forceinline__ unsigned cvt_pk_bf16(float lo, float hi) { f32x2 v = {lo, hi}; bf16x2_t b = __builtin_convertvector(v, bf16x2_t); return __builtin_bit_cast(unsigned, b); }
;     __device__ __forceinline__ void operator()(const f32x4 (&acc)[2][2][4][2], const u32x2 (&pf)[8], const g8::Unit& u, int wr, int wc, int fr, int fq) const {
;     ...
;                     const float rq = __builtin_amdgcn_rsqf(sq.x * (1.f / 256.f) + 1e-6f) * SCALE_A;
;                     const float* cp = cs + ((size_t)(row % S) * 16 + 4 * fq) * 2;
;                     const f32x4 c0 = *(const f32x4*)cp, c1 = *(const f32x4*)(cp + 4);
;                     const float cc[4] = {c0[0], c0[2], c1[0], c1[2]}, sn[4] = {c0[1], c0[3], c1[1], c1[3]};
;                     {   const f32x4 t1 = acc[ai][0][m][0] * rq, t2 = acc[ai][0][m][1] * rq;
;                         float o1[4], o2[4];
; #pragma unroll
;                         for (int j = 0; j < 4; ++j) { o1[j] = t1[j] * cc[j] - t2[j] * sn[j]; o2[j] = t1[j] * sn[j] + t2[j] * cc[j]; }
;                         bf16_t* qp = QA + (size_t)row * 384 + wc * 96 + 64 + 4 * fq;
;                         *(u32x2*)qp = (u32x2){cvt_pk_bf16(o1[0], o1[1]), cvt_pk_bf16(o1[2], o1[3])};
;                         *(u32x2*)(qp + 16) = (u32x2){cvt_pk_bf16(o2[0], o2[1]), cvt_pk_bf16(o2[2], o2[3])}; }
;                     {   const bf16_t* hp = H + (size_t)row * HP + C_KR + 4 * fq;
;                         const u32x2 a = *(const u32x2*)hp, b = *(const u32x2*)(hp + 16);
;                         const float t1[4] = {__uint_as_float(a.x << 16), __uint_as_float(a.x & 0xffff0000u), __uint_as_float(a.y << 16), __uint_as_float(a.y & 0xffff0000u)};
;                         const float t2[4] = {__uint_as_float(b.x << 16), __uint_as_float(b.x & 0xffff0000u), __uint_as_float(b.y << 16), __uint_as_float(b.y & 0xffff0000u)};
;                         float o1[4], o2[4];
; #pragma unroll
;                         for (int j = 0; j < 4; ++j) { o1[j] = t1[j] * cc[j] - t2[j] * sn[j]; o2[j] = t1[j] * sn[j] + t2[j] * cc[j]; }
;                         bf16_t* kp = KA + (size_t)row * 384 + wc * 96 + 64 + 4 * fq;
;                         *(u32x2*)kp = (u32x2){cvt_pk_bf16(o1[0], o1[1]), cvt_pk_bf16(o1[2], o1[3])};
;                         *(u32x2*)(kp + 16) = (u32x2){cvt_pk_bf16(o2[0], o2[1]), cvt_pk_bf16(o2[2], o2[3])}; }
	ds_bpermute_b32 v206, v141, v206
	ds_bpermute_b32 v207, v141, v207
	ds_bpermute_b32 v208, v141, v208
	ds_bpermute_b32 v209, v141, v209
	ds_bpermute_b32 v210, v141, v210
	ds_bpermute_b32 v211, v141, v211
	ds_bpermute_b32 v212, v141, v212
	ds_bpermute_b32 v213, v141, v213
	ds_bpermute_b32 v214, v141, v214
	ds_bpermute_b32 v215, v141, v215
	ds_bpermute_b32 v216, v141, v216
	ds_bpermute_b32 v217, v141, v217
	s_waitcnt lgkmcnt(0)
	v_mov_b64_e32 v[132:133], v[206:207]
	v_mov_b64_e32 v[134:135], v[208:209]
	v_mov_b64_e32 v[136:137], v[210:211]
	v_mov_b64_e32 v[138:139], v[212:213]
	v_pk_mul_f32 v[154:155], v[150:151], v[124:125] op_sel_hi:[0,1]
	v_pk_mul_f32 v[152:153], v[150:151], v[128:129] op_sel_hi:[0,1]
	v_pk_mul_f32 v[184:185], v[150:151], v[126:127] op_sel_hi:[0,1]
	v_mov_b32_e32 v178, v137
	v_mov_b32_e32 v137, v138
	v_mov_b32_e32 v179, v139
	v_pk_mul_f32 v[138:139], v[154:155], v[136:137]
	s_nop 0
	v_pk_fma_f32 v[180:181], v[152:153], v[178:179], v[138:139]
	v_pk_mul_f32 v[138:139], v[154:155], v[178:179]
	v_pk_mul_f32 v[154:155], v[150:151], v[130:131] op_sel_hi:[0,1]
	v_pk_fma_f32 v[152:153], v[152:153], v[136:137], v[138:139] neg_lo:[0,0,1] neg_hi:[0,0,1]
	v_mov_b32_e32 v138, v133
	v_mov_b32_e32 v139, v135
	v_mov_b32_e32 v133, v134
	v_pk_mul_f32 v[134:135], v[184:185], v[132:133]
	v_pk_mul_f32 v[184:185], v[184:185], v[138:139]
	v_pk_fma_f32 v[134:135], v[154:155], v[138:139], v[134:135]
	v_pk_fma_f32 v[154:155], v[154:155], v[132:133], v[184:185] neg_lo:[0,0,1] neg_hi:[0,0,1]
	v_mov_b64_e32 v[184:185], s[54:55]
	v_mad_i64_i32 v[184:185], s[14:15], v164, s0, v[184:185]
	v_lshl_add_u64 v[184:185], v[184:185], 0, v[186:187]
	v_cvt_pk_bf16_f32 v152, v152, v153
	v_cvt_pk_bf16_f32 v153, v154, v155
	v_cvt_pk_bf16_f32 v147, v134, v135
	v_mov_b64_e32 v[134:135], s[44:45]
	v_cvt_pk_bf16_f32 v146, v180, v181
	v_mad_i64_i32 v[134:135], s[14:15], v164, s33, v[134:135]
	ds_bpermute_b32 v152, v140, v152
	ds_bpermute_b32 v153, v140, v153
	ds_bpermute_b32 v146, v140, v146
	ds_bpermute_b32 v147, v140, v147
	v_lshl_add_u64 v[156:157], v[144:145], 0, v[184:185]
	s_waitcnt lgkmcnt(0)
	global_store_dwordx2 v[156:157], v[152:153], off offset:128
	global_store_dwordx2 v[156:157], v[146:147], off offset:160
	v_lshl_add_u64 v[134:135], v[134:135], 0, v[186:187]
	s_waitcnt vmcnt(14)
	v_mov_b64_e32 v[152:153], v[214:215]
	v_mov_b64_e32 v[134:135], v[216:217]
	v_lshlrev_b32_e32 v154, 16, v152
	v_lshlrev_b32_e32 v180, 16, v134
	v_and_b32_e32 v181, 0xffff0000, v134
	v_and_b32_e32 v155, 0xffff0000, v152
	v_pk_mul_f32 v[184:185], v[136:137], v[180:181]
	v_lshlrev_b32_e32 v134, 16, v135
	v_pk_fma_f32 v[184:185], v[178:179], v[154:155], v[184:185]
	v_pk_mul_f32 v[178:179], v[178:179], v[180:181]
	v_and_b32_e32 v135, 0xffff0000, v135
	v_pk_fma_f32 v[136:137], v[136:137], v[154:155], v[178:179] neg_lo:[0,0,1] neg_hi:[0,0,1]
	v_lshlrev_b32_e32 v152, 16, v153
	v_and_b32_e32 v153, 0xffff0000, v153
	v_pk_mul_f32 v[154:155], v[132:133], v[134:135]
	v_pk_mul_f32 v[134:135], v[138:139], v[134:135]
	v_pk_fma_f32 v[154:155], v[138:139], v[152:153], v[154:155]
	v_pk_fma_f32 v[132:133], v[132:133], v[152:153], v[134:135] neg_lo:[0,0,1] neg_hi:[0,0,1]
	v_mov_b64_e32 v[134:135], s[56:57]
	v_mad_i64_i32 v[134:135], s[14:15], v164, s0, v[134:135]
	v_lshl_add_u64 v[134:135], v[134:135], 0, v[186:187]
	v_cvt_pk_bf16_f32 v136, v136, v137
	v_cvt_pk_bf16_f32 v137, v132, v133
	v_cvt_pk_bf16_f32 v132, v184, v185
	v_cvt_pk_bf16_f32 v133, v154, v155
	ds_bpermute_b32 v136, v140, v136
	ds_bpermute_b32 v137, v140, v137
	ds_bpermute_b32 v132, v140, v132
	ds_bpermute_b32 v133, v140, v133
	v_lshl_add_u64 v[156:157], v[144:145], 0, v[134:135]
	s_waitcnt lgkmcnt(0)
	global_store_dwordx2 v[156:157], v[136:137], off offset:128
	global_store_dwordx2 v[156:157], v[132:133], off offset:160
	s_mov_b64 s[14:15], 0

; __device__ __forceinline__ unsigned cvt_pk_bf16(float lo, float hi) { f32x2 v = {lo, hi}; bf16x2_t b = __builtin_convertvector(v, bf16x2_t); return __builtin_bit_cast(unsigned, b); }
;     __device__ __forceinline__ void operator()(const f32x4 (&acc)[2][2][4][2], const u32x2 (&pf)[8], const g8::Unit& u, int wr, int wc, int fr, int fq) const {
;     ...
;                 if (u.pn == 1) {
;                     const float rq = __builtin_amdgcn_rsqf(sq.x * (1.f / 256.f) + 1e-6f) * SCALE_A;
;                     const float* cp = cs + ((size_t)(row % S) * 16 + 4 * fq) * 2;
;                     const f32x4 c0 = *(const f32x4*)cp, c1 = *(const f32x4*)(cp + 4);
;                     const float cc[4] = {c0[0], c0[2], c1[0], c1[2]}, sn[4] = {c0[1], c0[3], c1[1], c1[3]};
;                     {   const f32x4 t1 = acc[ai][0][m][0] * rq, t2 = acc[ai][0][m][1] * rq;
;                         float o1[4], o2[4];
; #pragma unroll
;                         for (int j = 0; j < 4; ++j) { o1[j] = t1[j] * cc[j] - t2[j] * sn[j]; o2[j] = t1[j] * sn[j] + t2[j] * cc[j]; }
;                         bf16_t* qp = QA + (size_t)row * 384 + wc * 96 + 64 + 4 * fq;
;                         *(u32x2*)qp = (u32x2){cvt_pk_bf16(o1[0], o1[1]), cvt_pk_bf16(o1[2], o1[3])};
;                         *(u32x2*)(qp + 16) = (u32x2){cvt_pk_bf16(o2[0], o2[1]), cvt_pk_bf16(o2[2], o2[3])}; }
;                     {   const bf16_t* hp = H + (size_t)row * HP + C_KR + 4 * fq;
;                         const u32x2 a = *(const u32x2*)hp, b = *(const u32x2*)(hp + 16);
;                         const float t1[4] = {__uint_as_float(a.x << 16), __uint_as_float(a.x & 0xffff0000u), __uint_as_float(a.y << 16), __uint_as_float(a.y & 0xffff0000u)};
;                         const float t2[4] = {__uint_as_float(b.x << 16), __uint_as_float(b.x & 0xffff0000u), __uint_as_float(b.y << 16), __uint_as_float(b.y & 0xffff0000u)};
;                         float o1[4], o2[4];
; #pragma unroll
;                         for (int j = 0; j < 4; ++j) { o1[j] = t1[j] * cc[j] - t2[j] * sn[j]; o2[j] = t1[j] * sn[j] + t2[j] * cc[j]; }
;                         bf16_t* kp = KA + (size_t)row * 384 + wc * 96 + 64 + 4 * fq;
;                         *(u32x2*)kp = (u32x2){cvt_pk_bf16(o1[0], o1[1]), cvt_pk_bf16(o1[2], o1[3])};
;                         *(u32x2*)(kp + 16) = (u32x2){cvt_pk_bf16(o2[0], o2[1]), cvt_pk_bf16(o2[2], o2[3])}; }
.LBB0_568:
	s_cmp_eq_u32 s67, 1
	s_mov_b64 s[14:15], -1
	s_cbranch_scc0 .LBB0_570
	v_fmamk_f32 v116, v174, 0x3b800000, v246
	v_rsq_f32_e32 v116, v116
	v_lshlrev_b32_e32 v136, 1, v5
	v_mov_b32_e32 v137, v31
	v_mul_f32_e32 v128, 0x3e16c740, v116
	v_ashrrev_i32_e32 v116, 31, v124
	v_lshrrev_b32_e32 v116, 19, v116
	v_add_u32_e32 v116, v124, v116
	v_and_b32_e32 v116, 0xffffe000, v116
	v_sub_u32_e32 v116, v124, v116
	v_ashrrev_i32_e32 v117, 31, v116
	v_lshlrev_b64 v[116:117], 7, v[116:117]
	v_lshl_add_u64 v[116:117], s[46:47], 0, v[116:117]
	v_lshl_add_u64 v[120:121], v[116:117], 0, v[30:31]
	s_waitcnt vmcnt(12)
	ds_bpermute_b32 v218, v141, v218
	ds_bpermute_b32 v219, v141, v219
	ds_bpermute_b32 v220, v141, v220
	ds_bpermute_b32 v221, v141, v221
	ds_bpermute_b32 v222, v141, v222
	ds_bpermute_b32 v223, v141, v223
	ds_bpermute_b32 v224, v141, v224
	ds_bpermute_b32 v225, v141, v225
	ds_bpermute_b32 v226, v141, v226
	ds_bpermute_b32 v227, v141, v227
	ds_bpermute_b32 v228, v141, v228
	ds_bpermute_b32 v229, v141, v229
	s_waitcnt lgkmcnt(0)
	v_mov_b64_e32 v[116:117], v[218:219]
	v_mov_b64_e32 v[118:119], v[220:221]
	v_mov_b64_e32 v[120:121], v[222:223]
	v_mov_b64_e32 v[122:123], v[224:225]
	v_pk_mul_f32 v[132:133], v[128:129], v[108:109] op_sel_hi:[0,1]
	v_pk_mul_f32 v[130:131], v[128:129], v[112:113] op_sel_hi:[0,1]
	v_mov_b32_e32 v126, v121
	v_mov_b32_e32 v121, v122
	v_mov_b32_e32 v127, v123
	v_pk_mul_f32 v[122:123], v[132:133], v[120:121]
	s_nop 0
	v_pk_fma_f32 v[134:135], v[130:131], v[126:127], v[122:123]
	v_pk_mul_f32 v[122:123], v[132:133], v[126:127]
	v_pk_mul_f32 v[132:133], v[128:129], v[114:115] op_sel_hi:[0,1]
	v_pk_fma_f32 v[130:131], v[130:131], v[120:121], v[122:123] neg_lo:[0,0,1] neg_hi:[0,0,1]
	v_pk_mul_f32 v[128:129], v[128:129], v[110:111] op_sel_hi:[0,1]
	v_mov_b32_e32 v122, v117
	v_mov_b32_e32 v123, v119
	v_mov_b32_e32 v117, v118
	v_pk_mul_f32 v[118:119], v[128:129], v[116:117]
	v_pk_mul_f32 v[128:129], v[128:129], v[122:123]
	v_pk_fma_f32 v[118:119], v[132:133], v[122:123], v[118:119]
	v_pk_fma_f32 v[128:129], v[132:133], v[116:117], v[128:129] neg_lo:[0,0,1] neg_hi:[0,0,1]
	v_mov_b64_e32 v[132:133], s[54:55]
	v_mad_i64_i32 v[132:133], s[14:15], v124, s0, v[132:133]
	v_cvt_pk_bf16_f32 v130, v130, v131
	v_cvt_pk_bf16_f32 v131, v128, v129
	v_cvt_pk_bf16_f32 v129, v118, v119
	v_mov_b64_e32 v[118:119], s[44:45]
	v_lshl_add_u64 v[132:133], v[132:133], 0, v[136:137]
	v_cvt_pk_bf16_f32 v128, v134, v135
	v_mad_i64_i32 v[118:119], s[14:15], v124, s33, v[118:119]
	ds_bpermute_b32 v130, v140, v130
	ds_bpermute_b32 v131, v140, v131
	ds_bpermute_b32 v128, v140, v128
	ds_bpermute_b32 v129, v140, v129
	v_lshl_add_u64 v[156:157], v[144:145], 0, v[132:133]
	s_waitcnt lgkmcnt(0)
	global_store_dwordx2 v[156:157], v[130:131], off offset:128
	global_store_dwordx2 v[156:157], v[128:129], off offset:160
	v_lshl_add_u64 v[118:119], v[118:119], 0, v[136:137]
	s_waitcnt vmcnt(14)
	v_mov_b64_e32 v[128:129], v[226:227]
	v_mov_b64_e32 v[118:119], v[228:229]
	v_lshlrev_b32_e32 v130, 16, v128
	v_lshlrev_b32_e32 v132, 16, v118
	v_and_b32_e32 v133, 0xffff0000, v118
	v_and_b32_e32 v131, 0xffff0000, v128
	v_pk_mul_f32 v[134:135], v[120:121], v[132:133]
	v_lshlrev_b32_e32 v118, 16, v119
	v_pk_fma_f32 v[134:135], v[126:127], v[130:131], v[134:135]
	v_pk_mul_f32 v[126:127], v[126:127], v[132:133]
	v_and_b32_e32 v119, 0xffff0000, v119
	v_pk_fma_f32 v[120:121], v[120:121], v[130:131], v[126:127] neg_lo:[0,0,1] neg_hi:[0,0,1]
	v_lshlrev_b32_e32 v126, 16, v129
	v_and_b32_e32 v127, 0xffff0000, v129
	v_pk_mul_f32 v[128:129], v[116:117], v[118:119]
	v_pk_mul_f32 v[118:119], v[122:123], v[118:119]
	v_pk_fma_f32 v[128:129], v[122:123], v[126:127], v[128:129]
	v_pk_fma_f32 v[116:117], v[116:117], v[126:127], v[118:119] neg_lo:[0,0,1] neg_hi:[0,0,1]
	v_mov_b64_e32 v[118:119], s[56:57]
	v_mad_i64_i32 v[118:119], s[14:15], v124, s0, v[118:119]
	v_lshl_add_u64 v[118:119], v[118:119], 0, v[136:137]
	v_cvt_pk_bf16_f32 v120, v120, v121
	v_cvt_pk_bf16_f32 v121, v116, v117
	v_cvt_pk_bf16_f32 v116, v134, v135
	v_cvt_pk_bf16_f32 v117, v128, v129
	ds_bpermute_b32 v120, v140, v120
	ds_bpermute_b32 v121, v140, v121
	ds_bpermute_b32 v116, v140, v116
	ds_bpermute_b32 v117, v140, v117
	v_lshl_add_u64 v[156:157], v[144:145], 0, v[118:119]
	s_waitcnt lgkmcnt(0)
	global_store_dwordx2 v[156:157], v[120:121], off offset:128
	global_store_dwordx2 v[156:157], v[116:117], off offset:160
	s_mov_b64 s[14:15], 0

; __device__ __forceinline__ unsigned cvt_pk_bf16(float lo, float hi) { f32x2 v = {lo, hi}; bf16x2_t b = __builtin_convertvector(v, bf16x2_t); return __builtin_bit_cast(unsigned, b); }
;     __device__ __forceinline__ void operator()(const f32x4 (&acc)[2][2][4][2], const u32x2 (&pf)[8], const g8::Unit& u, int wr, int wc, int fr, int fq) const {
;     ...
;                 if (u.pn == 1) {
;                     const float rq = __builtin_amdgcn_rsqf(sq.x * (1.f / 256.f) + 1e-6f) * SCALE_A;
;                     const float* cp = cs + ((size_t)(row % S) * 16 + 4 * fq) * 2;
;                     const f32x4 c0 = *(const f32x4*)cp, c1 = *(const f32x4*)(cp + 4);
;                     const float cc[4] = {c0[0], c0[2], c1[0], c1[2]}, sn[4] = {c0[1], c0[3], c1[1], c1[3]};
;                     {   const f32x4 t1 = acc[ai][0][m][0] * rq, t2 = acc[ai][0][m][1] * rq;
;                         float o1[4], o2[4];
; #pragma unroll
;                         for (int j = 0; j < 4; ++j) { o1[j] = t1[j] * cc[j] - t2[j] * sn[j]; o2[j] = t1[j] * sn[j] + t2[j] * cc[j]; }
;                         bf16_t* qp = QA + (size_t)row * 384 + wc * 96 + 64 + 4 * fq;
;                         *(u32x2*)qp = (u32x2){cvt_pk_bf16(o1[0], o1[1]), cvt_pk_bf16(o1[2], o1[3])};
;                         *(u32x2*)(qp + 16) = (u32x2){cvt_pk_bf16(o2[0], o2[1]), cvt_pk_bf16(o2[2], o2[3])}; }
;                     {   const bf16_t* hp = H + (size_t)row * HP + C_KR + 4 * fq;
;                         const u32x2 a = *(const u32x2*)hp, b = *(const u32x2*)(hp + 16);
;                         const float t1[4] = {__uint_as_float(a.x << 16), __uint_as_float(a.x & 0xffff0000u), __uint_as_float(a.y << 16), __uint_as_float(a.y & 0xffff0000u)};
;                         const float t2[4] = {__uint_as_float(b.x << 16), __uint_as_float(b.x & 0xffff0000u), __uint_as_float(b.y << 16), __uint_as_float(b.y & 0xffff0000u)};
;                         float o1[4], o2[4];
; #pragma unroll
;                         for (int j = 0; j < 4; ++j) { o1[j] = t1[j] * cc[j] - t2[j] * sn[j]; o2[j] = t1[j] * sn[j] + t2[j] * cc[j]; }
;                         bf16_t* kp = KA + (size_t)row * 384 + wc * 96 + 64 + 4 * fq;
;                         *(u32x2*)kp = (u32x2){cvt_pk_bf16(o1[0], o1[1]), cvt_pk_bf16(o1[2], o1[3])};
;                         *(u32x2*)(kp + 16) = (u32x2){cvt_pk_bf16(o2[0], o2[1]), cvt_pk_bf16(o2[2], o2[3])}; }
.LBB0_595:
	s_cmp_eq_u32 s67, 1
	s_mov_b64 s[14:15], -1
	s_cbranch_scc0 .LBB0_597
	v_fmamk_f32 v100, v172, 0x3b800000, v246
	v_rsq_f32_e32 v100, v100
	v_lshlrev_b32_e32 v120, 1, v5
	v_mov_b32_e32 v121, v31
	v_mul_f32_e32 v112, 0x3e16c740, v100
	v_ashrrev_i32_e32 v100, 31, v108
	v_lshrrev_b32_e32 v100, 19, v100
	v_add_u32_e32 v100, v108, v100
	v_and_b32_e32 v100, 0xffffe000, v100
	v_sub_u32_e32 v100, v108, v100
	v_ashrrev_i32_e32 v101, 31, v100
	v_lshlrev_b64 v[100:101], 7, v[100:101]
	v_lshl_add_u64 v[100:101], s[46:47], 0, v[100:101]
	v_lshl_add_u64 v[104:105], v[100:101], 0, v[30:31]
	s_waitcnt vmcnt(12)
	ds_bpermute_b32 v230, v141, v230
	ds_bpermute_b32 v231, v141, v231
	ds_bpermute_b32 v232, v141, v232
	ds_bpermute_b32 v233, v141, v233
	ds_bpermute_b32 v234, v141, v234
	ds_bpermute_b32 v235, v141, v235
	ds_bpermute_b32 v236, v141, v236
	ds_bpermute_b32 v237, v141, v237
	ds_bpermute_b32 v238, v141, v238
	ds_bpermute_b32 v239, v141, v239
	ds_bpermute_b32 v240, v141, v240
	ds_bpermute_b32 v241, v141, v241
	s_waitcnt lgkmcnt(0)
	v_mov_b64_e32 v[100:101], v[230:231]
	v_mov_b64_e32 v[102:103], v[232:233]
	v_mov_b64_e32 v[104:105], v[234:235]
	v_mov_b64_e32 v[106:107], v[236:237]
	v_pk_mul_f32 v[116:117], v[112:113], v[92:93] op_sel_hi:[0,1]
	v_pk_mul_f32 v[114:115], v[112:113], v[96:97] op_sel_hi:[0,1]
	v_mov_b32_e32 v110, v105
	v_mov_b32_e32 v105, v106
	v_mov_b32_e32 v111, v107
	v_pk_mul_f32 v[106:107], v[116:117], v[104:105]
	s_nop 0
	v_pk_fma_f32 v[118:119], v[114:115], v[110:111], v[106:107]
	v_pk_mul_f32 v[106:107], v[116:117], v[110:111]
	v_pk_mul_f32 v[116:117], v[112:113], v[98:99] op_sel_hi:[0,1]
	v_pk_fma_f32 v[114:115], v[114:115], v[104:105], v[106:107] neg_lo:[0,0,1] neg_hi:[0,0,1]
	v_pk_mul_f32 v[112:113], v[112:113], v[94:95] op_sel_hi:[0,1]
	v_mov_b32_e32 v106, v101
	v_mov_b32_e32 v107, v103
	v_mov_b32_e32 v101, v102
	v_pk_mul_f32 v[102:103], v[112:113], v[100:101]
	v_pk_mul_f32 v[112:113], v[112:113], v[106:107]
	v_pk_fma_f32 v[102:103], v[116:117], v[106:107], v[102:103]
	v_pk_fma_f32 v[112:113], v[116:117], v[100:101], v[112:113] neg_lo:[0,0,1] neg_hi:[0,0,1]
	v_mov_b64_e32 v[116:117], s[54:55]
	v_mad_i64_i32 v[116:117], s[14:15], v108, s0, v[116:117]
	v_cvt_pk_bf16_f32 v114, v114, v115
	v_cvt_pk_bf16_f32 v115, v112, v113
	v_cvt_pk_bf16_f32 v113, v102, v103
	v_mov_b64_e32 v[102:103], s[44:45]
	v_lshl_add_u64 v[116:117], v[116:117], 0, v[120:121]
	v_cvt_pk_bf16_f32 v112, v118, v119
	v_mad_i64_i32 v[102:103], s[14:15], v108, s33, v[102:103]
	ds_bpermute_b32 v114, v140, v114
	ds_bpermute_b32 v115, v140, v115
	ds_bpermute_b32 v112, v140, v112
	ds_bpermute_b32 v113, v140, v113
	v_lshl_add_u64 v[156:157], v[144:145], 0, v[116:117]
	s_waitcnt lgkmcnt(0)
	global_store_dwordx2 v[156:157], v[114:115], off offset:128
	global_store_dwordx2 v[156:157], v[112:113], off offset:160
	v_lshl_add_u64 v[102:103], v[102:103], 0, v[120:121]
	s_waitcnt vmcnt(14)
	v_mov_b64_e32 v[112:113], v[238:239]
	v_mov_b64_e32 v[102:103], v[240:241]
	v_lshlrev_b32_e32 v114, 16, v112
	v_lshlrev_b32_e32 v116, 16, v102
	v_and_b32_e32 v117, 0xffff0000, v102
	v_and_b32_e32 v115, 0xffff0000, v112
	v_pk_mul_f32 v[118:119], v[104:105], v[116:117]
	v_lshlrev_b32_e32 v102, 16, v103
	v_pk_fma_f32 v[118:119], v[110:111], v[114:115], v[118:119]
	v_pk_mul_f32 v[110:111], v[110:111], v[116:117]
	v_and_b32_e32 v103, 0xffff0000, v103
	v_pk_fma_f32 v[104:105], v[104:105], v[114:115], v[110:111] neg_lo:[0,0,1] neg_hi:[0,0,1]
	v_lshlrev_b32_e32 v110, 16, v113
	v_and_b32_e32 v111, 0xffff0000, v113
	v_pk_mul_f32 v[112:113], v[100:101], v[102:103]
	v_pk_mul_f32 v[102:103], v[106:107], v[102:103]
	v_pk_fma_f32 v[112:113], v[106:107], v[110:111], v[112:113]
	v_pk_fma_f32 v[100:101], v[100:101], v[110:111], v[102:103] neg_lo:[0,0,1] neg_hi:[0,0,1]
	v_mov_b64_e32 v[102:103], s[56:57]
	v_mad_i64_i32 v[102:103], s[14:15], v108, s0, v[102:103]
	v_lshl_add_u64 v[102:103], v[102:103], 0, v[120:121]
	v_cvt_pk_bf16_f32 v104, v104, v105
	v_cvt_pk_bf16_f32 v105, v100, v101
	v_cvt_pk_bf16_f32 v100, v118, v119
	v_cvt_pk_bf16_f32 v101, v112, v113
	ds_bpermute_b32 v104, v140, v104
	ds_bpermute_b32 v105, v140, v105
	ds_bpermute_b32 v100, v140, v100
	ds_bpermute_b32 v101, v140, v101
	v_lshl_add_u64 v[156:157], v[144:145], 0, v[102:103]
	s_waitcnt lgkmcnt(0)
	global_store_dwordx2 v[156:157], v[104:105], off offset:128
	global_store_dwordx2 v[156:157], v[100:101], off offset:160
	s_mov_b64 s[14:15], 0

; __device__ __forceinline__ unsigned cvt_pk_bf16(float lo, float hi) { f32x2 v = {lo, hi}; bf16x2_t b = __builtin_convertvector(v, bf16x2_t); return __builtin_bit_cast(unsigned, b); }
;     __device__ __forceinline__ void operator()(const f32x4 (&acc)[2][2][4][2], const u32x2 (&pf)[8], const g8::Unit& u, int wr, int wc, int fr, int fq) const {
;     ...
;                 if (u.pn == 1) {
;                     const float rq = __builtin_amdgcn_rsqf(sq.x * (1.f / 256.f) + 1e-6f) * SCALE_A;
;                     const float* cp = cs + ((size_t)(row % S) * 16 + 4 * fq) * 2;
;                     const f32x4 c0 = *(const f32x4*)cp, c1 = *(const f32x4*)(cp + 4);
;                     const float cc[4] = {c0[0], c0[2], c1[0], c1[2]}, sn[4] = {c0[1], c0[3], c1[1], c1[3]};
;                     {   const f32x4 t1 = acc[ai][0][m][0] * rq, t2 = acc[ai][0][m][1] * rq;
;                         float o1[4], o2[4];
; #pragma unroll
;                         for (int j = 0; j < 4; ++j) { o1[j] = t1[j] * cc[j] - t2[j] * sn[j]; o2[j] = t1[j] * sn[j] + t2[j] * cc[j]; }
;                         bf16_t* qp = QA + (size_t)row * 384 + wc * 96 + 64 + 4 * fq;
;                         *(u32x2*)qp = (u32x2){cvt_pk_bf16(o1[0], o1[1]), cvt_pk_bf16(o1[2], o1[3])};
;                         *(u32x2*)(qp + 16) = (u32x2){cvt_pk_bf16(o2[0], o2[1]), cvt_pk_bf16(o2[2], o2[3])}; }
;                     {   const bf16_t* hp = H + (size_t)row * HP + C_KR + 4 * fq;
;                         const u32x2 a = *(const u32x2*)hp, b = *(const u32x2*)(hp + 16);
;                         const float t1[4] = {__uint_as_float(a.x << 16), __uint_as_float(a.x & 0xffff0000u), __uint_as_float(a.y << 16), __uint_as_float(a.y & 0xffff0000u)};
;                         const float t2[4] = {__uint_as_float(b.x << 16), __uint_as_float(b.x & 0xffff0000u), __uint_as_float(b.y << 16), __uint_as_float(b.y & 0xffff0000u)};
;                         float o1[4], o2[4];
; #pragma unroll
;                         for (int j = 0; j < 4; ++j) { o1[j] = t1[j] * cc[j] - t2[j] * sn[j]; o2[j] = t1[j] * sn[j] + t2[j] * cc[j]; }
;                         bf16_t* kp = KA + (size_t)row * 384 + wc * 96 + 64 + 4 * fq;
;                         *(u32x2*)kp = (u32x2){cvt_pk_bf16(o1[0], o1[1]), cvt_pk_bf16(o1[2], o1[3])};
;                         *(u32x2*)(kp + 16) = (u32x2){cvt_pk_bf16(o2[0], o2[1]), cvt_pk_bf16(o2[2], o2[3])}; }
.LBB0_622:
	s_cmp_eq_u32 s67, 1
	s_mov_b64 s[14:15], -1
	s_cbranch_scc0 .LBB0_624
	v_fmamk_f32 v84, v170, 0x3b800000, v246
	v_rsq_f32_e32 v84, v84
	v_lshlrev_b32_e32 v104, 1, v5
	v_mov_b32_e32 v105, v31
	v_mul_f32_e32 v96, 0x3e16c740, v84
	v_ashrrev_i32_e32 v84, 31, v92
	v_lshrrev_b32_e32 v84, 19, v84
	v_add_u32_e32 v84, v92, v84
	v_and_b32_e32 v84, 0xffffe000, v84
	v_sub_u32_e32 v84, v92, v84
	v_ashrrev_i32_e32 v85, 31, v84
	v_lshlrev_b64 v[84:85], 7, v[84:85]
	v_lshl_add_u64 v[84:85], s[46:47], 0, v[84:85]
	v_lshl_add_u64 v[88:89], v[84:85], 0, v[30:31]
	s_waitcnt vmcnt(12)
	ds_bpermute_b32 v242, v141, v242
	ds_bpermute_b32 v243, v141, v243
	ds_bpermute_b32 v244, v141, v244
	ds_bpermute_b32 v245, v141, v245
	ds_bpermute_b32 v188, v141, v188
	ds_bpermute_b32 v189, v141, v189
	ds_bpermute_b32 v190, v141, v190
	ds_bpermute_b32 v191, v141, v191
	ds_bpermute_b32 v192, v141, v192
	ds_bpermute_b32 v193, v141, v193
	ds_bpermute_b32 v194, v141, v194
	ds_bpermute_b32 v195, v141, v195
	s_waitcnt lgkmcnt(0)
	v_mov_b64_e32 v[84:85], v[242:243]
	v_mov_b64_e32 v[86:87], v[244:245]
	v_mov_b64_e32 v[88:89], v[188:189]
	v_mov_b64_e32 v[90:91], v[190:191]
	v_pk_mul_f32 v[100:101], v[96:97], v[76:77] op_sel_hi:[0,1]
	v_pk_mul_f32 v[98:99], v[96:97], v[80:81] op_sel_hi:[0,1]
	v_mov_b32_e32 v94, v89
	v_mov_b32_e32 v89, v90
	v_mov_b32_e32 v95, v91
	v_pk_mul_f32 v[90:91], v[100:101], v[88:89]
	s_nop 0
	v_pk_fma_f32 v[102:103], v[98:99], v[94:95], v[90:91]
	v_pk_mul_f32 v[90:91], v[100:101], v[94:95]
	v_pk_mul_f32 v[100:101], v[96:97], v[82:83] op_sel_hi:[0,1]
	v_pk_fma_f32 v[98:99], v[98:99], v[88:89], v[90:91] neg_lo:[0,0,1] neg_hi:[0,0,1]
	v_pk_mul_f32 v[96:97], v[96:97], v[78:79] op_sel_hi:[0,1]
	v_mov_b32_e32 v90, v85
	v_mov_b32_e32 v91, v87
	v_mov_b32_e32 v85, v86
	v_pk_mul_f32 v[86:87], v[96:97], v[84:85]
	v_pk_mul_f32 v[96:97], v[96:97], v[90:91]
	v_pk_fma_f32 v[86:87], v[100:101], v[90:91], v[86:87]
	v_pk_fma_f32 v[96:97], v[100:101], v[84:85], v[96:97] neg_lo:[0,0,1] neg_hi:[0,0,1]
	v_mov_b64_e32 v[100:101], s[54:55]
	v_mad_i64_i32 v[100:101], s[14:15], v92, s0, v[100:101]
	v_cvt_pk_bf16_f32 v98, v98, v99
	v_cvt_pk_bf16_f32 v99, v96, v97
	v_cvt_pk_bf16_f32 v97, v86, v87
	v_mov_b64_e32 v[86:87], s[44:45]
	v_lshl_add_u64 v[100:101], v[100:101], 0, v[104:105]
	v_cvt_pk_bf16_f32 v96, v102, v103
	v_mad_i64_i32 v[86:87], s[14:15], v92, s33, v[86:87]
	ds_bpermute_b32 v98, v140, v98
	ds_bpermute_b32 v99, v140, v99
	ds_bpermute_b32 v96, v140, v96
	ds_bpermute_b32 v97, v140, v97
	v_lshl_add_u64 v[156:157], v[144:145], 0, v[100:101]
	s_waitcnt lgkmcnt(0)
	global_store_dwordx2 v[156:157], v[98:99], off offset:128
	global_store_dwordx2 v[156:157], v[96:97], off offset:160
	v_lshl_add_u64 v[86:87], v[86:87], 0, v[104:105]
	s_waitcnt vmcnt(14)
	v_mov_b64_e32 v[96:97], v[192:193]
	v_mov_b64_e32 v[86:87], v[194:195]
	v_lshlrev_b32_e32 v98, 16, v96
	v_lshlrev_b32_e32 v100, 16, v86
	v_and_b32_e32 v101, 0xffff0000, v86
	v_and_b32_e32 v99, 0xffff0000, v96
	v_pk_mul_f32 v[102:103], v[88:89], v[100:101]
	v_lshlrev_b32_e32 v86, 16, v87
	v_pk_fma_f32 v[102:103], v[94:95], v[98:99], v[102:103]
	v_pk_mul_f32 v[94:95], v[94:95], v[100:101]
	v_and_b32_e32 v87, 0xffff0000, v87
	v_pk_fma_f32 v[88:89], v[88:89], v[98:99], v[94:95] neg_lo:[0,0,1] neg_hi:[0,0,1]
	v_lshlrev_b32_e32 v94, 16, v97
	v_and_b32_e32 v95, 0xffff0000, v97
	v_pk_mul_f32 v[96:97], v[84:85], v[86:87]
	v_pk_mul_f32 v[86:87], v[90:91], v[86:87]
	v_pk_fma_f32 v[96:97], v[90:91], v[94:95], v[96:97]
	v_pk_fma_f32 v[84:85], v[84:85], v[94:95], v[86:87] neg_lo:[0,0,1] neg_hi:[0,0,1]
	v_mov_b64_e32 v[86:87], s[56:57]
	v_mad_i64_i32 v[86:87], s[14:15], v92, s0, v[86:87]
	v_lshl_add_u64 v[86:87], v[86:87], 0, v[104:105]
	v_cvt_pk_bf16_f32 v88, v88, v89
	v_cvt_pk_bf16_f32 v89, v84, v85
	v_cvt_pk_bf16_f32 v84, v102, v103
	v_cvt_pk_bf16_f32 v85, v96, v97
	ds_bpermute_b32 v88, v140, v88
	ds_bpermute_b32 v89, v140, v89
	ds_bpermute_b32 v84, v140, v84
	ds_bpermute_b32 v85, v140, v85
	v_lshl_add_u64 v[156:157], v[144:145], 0, v[86:87]
	s_waitcnt lgkmcnt(0)
	global_store_dwordx2 v[156:157], v[88:89], off offset:128
	global_store_dwordx2 v[156:157], v[84:85], off offset:160
	s_mov_b64 s[14:15], 0

; __device__ __forceinline__ unsigned cvt_pk_bf16(float lo, float hi) { f32x2 v = {lo, hi}; bf16x2_t b = __builtin_convertvector(v, bf16x2_t); return __builtin_bit_cast(unsigned, b); }
;     __device__ __forceinline__ void operator()(const f32x4 (&acc)[2][2][4][2], const u32x2 (&pf)[8], const g8::Unit& u, int wr, int wc, int fr, int fq) const {
;     ...
;                 if (u.pn == 1) {
;                     const float rq = __builtin_amdgcn_rsqf(sq.x * (1.f / 256.f) + 1e-6f) * SCALE_A;
;                     const float* cp = cs + ((size_t)(row % S) * 16 + 4 * fq) * 2;
;                     const f32x4 c0 = *(const f32x4*)cp, c1 = *(const f32x4*)(cp + 4);
;                     const float cc[4] = {c0[0], c0[2], c1[0], c1[2]}, sn[4] = {c0[1], c0[3], c1[1], c1[3]};
;                     {   const f32x4 t1 = acc[ai][0][m][0] * rq, t2 = acc[ai][0][m][1] * rq;
;                         float o1[4], o2[4];
; #pragma unroll
;                         for (int j = 0; j < 4; ++j) { o1[j] = t1[j] * cc[j] - t2[j] * sn[j]; o2[j] = t1[j] * sn[j] + t2[j] * cc[j]; }
;                         bf16_t* qp = QA + (size_t)row * 384 + wc * 96 + 64 + 4 * fq;
;                         *(u32x2*)qp = (u32x2){cvt_pk_bf16(o1[0], o1[1]), cvt_pk_bf16(o1[2], o1[3])};
;                         *(u32x2*)(qp + 16) = (u32x2){cvt_pk_bf16(o2[0], o2[1]), cvt_pk_bf16(o2[2], o2[3])}; }
;                     {   const bf16_t* hp = H + (size_t)row * HP + C_KR + 4 * fq;
;                         const u32x2 a = *(const u32x2*)hp, b = *(const u32x2*)(hp + 16);
.LBB0_649:
	s_cmp_eq_u32 s67, 1
	s_mov_b64 s[14:15], -1
	s_cbranch_scc0 .LBB0_651
	v_lshlrev_b32_e32 v198, 3, v143
	v_mov_b32_e32 v199, v31
	v_add_u32_e32 v4, 0x80, v164
	v_add_u32_e32 v4, v142, v4
	v_ashrrev_i32_e32 v196, 31, v4
	v_lshrrev_b32_e32 v196, 19, v196
	v_add_u32_e32 v196, v4, v196
	v_and_b32_e32 v196, 0xffffe000, v196
	v_sub_u32_e32 v196, v4, v196
	v_ashrrev_i32_e32 v197, 31, v196
	v_lshlrev_b64 v[196:197], 7, v[196:197]
	v_lshl_add_u64 v[196:197], s[46:47], 0, v[196:197]
	v_lshl_add_u64 v[196:197], v[198:199], 2, v[196:197]
	global_load_dwordx4 v[206:209], v[196:197], off offset:16
	global_load_dwordx4 v[210:213], v[196:197], off
	v_mov_b64_e32 v[196:197], s[44:45]
	v_mad_i64_i32 v[196:197], s[14:15], v4, s33, v[196:197]
	v_lshl_add_u64 v[196:197], v[196:197], 0, v[198:199]
	global_load_dwordx2 v[214:215], v[196:197], off offset:768
	global_load_dwordx2 v[216:217], v[196:197], off offset:800
	v_add_u32_e32 v4, 0x90, v164
	v_add_u32_e32 v4, v142, v4
	v_ashrrev_i32_e32 v196, 31, v4
	v_lshrrev_b32_e32 v196, 19, v196
	v_add_u32_e32 v196, v4, v196
	v_and_b32_e32 v196, 0xffffe000, v196
	v_sub_u32_e32 v196, v4, v196
	v_ashrrev_i32_e32 v197, 31, v196
	v_lshlrev_b64 v[196:197], 7, v[196:197]
	v_lshl_add_u64 v[196:197], s[46:47], 0, v[196:197]
	v_lshl_add_u64 v[196:197], v[198:199], 2, v[196:197]
	global_load_dwordx4 v[218:221], v[196:197], off offset:16
	global_load_dwordx4 v[222:225], v[196:197], off
	v_mov_b64_e32 v[196:197], s[44:45]
	v_mad_i64_i32 v[196:197], s[14:15], v4, s33, v[196:197]
	v_lshl_add_u64 v[196:197], v[196:197], 0, v[198:199]
	global_load_dwordx2 v[226:227], v[196:197], off offset:768
	global_load_dwordx2 v[228:229], v[196:197], off offset:800
	v_add_u32_e32 v4, 0xa0, v164
	v_add_u32_e32 v4, v142, v4
	v_ashrrev_i32_e32 v196, 31, v4
	v_lshrrev_b32_e32 v196, 19, v196
	v_add_u32_e32 v196, v4, v196
	v_and_b32_e32 v196, 0xffffe000, v196
	v_sub_u32_e32 v196, v4, v196
	v_ashrrev_i32_e32 v197, 31, v196
	v_lshlrev_b64 v[196:197], 7, v[196:197]
	v_lshl_add_u64 v[196:197], s[46:47], 0, v[196:197]
	v_lshl_add_u64 v[196:197], v[198:199], 2, v[196:197]
	global_load_dwordx4 v[230:233], v[196:197], off offset:16
	global_load_dwordx4 v[234:237], v[196:197], off
	v_mov_b64_e32 v[196:197], s[44:45]
	v_mad_i64_i32 v[196:197], s[14:15], v4, s33, v[196:197]
	v_lshl_add_u64 v[196:197], v[196:197], 0, v[198:199]
	global_load_dwordx2 v[238:239], v[196:197], off offset:768
	global_load_dwordx2 v[240:241], v[196:197], off offset:800
	v_add_u32_e32 v4, 0xb0, v164
	v_add_u32_e32 v4, v142, v4
	v_ashrrev_i32_e32 v196, 31, v4
	v_lshrrev_b32_e32 v196, 19, v196
	v_add_u32_e32 v196, v4, v196
	v_and_b32_e32 v196, 0xffffe000, v196
	v_sub_u32_e32 v196, v4, v196
	v_ashrrev_i32_e32 v197, 31, v196
	v_lshlrev_b64 v[196:197], 7, v[196:197]
	v_lshl_add_u64 v[196:197], s[46:47], 0, v[196:197]
	v_lshl_add_u64 v[196:197], v[198:199], 2, v[196:197]
	global_load_dwordx4 v[242:245], v[196:197], off offset:16
	global_load_dwordx4 v[188:191], v[196:197], off
	v_mov_b64_e32 v[196:197], s[44:45]
	v_mad_i64_i32 v[196:197], s[14:15], v4, s33, v[196:197]
	v_lshl_add_u64 v[196:197], v[196:197], 0, v[198:199]
	global_load_dwordx2 v[192:193], v[196:197], off offset:768
	global_load_dwordx2 v[194:195], v[196:197], off offset:800
	v_fmamk_f32 v68, v168, 0x3b800000, v246
	v_rsq_f32_e32 v68, v68
	v_lshlrev_b32_e32 v88, 1, v5
	v_mov_b32_e32 v89, v31
	v_mul_f32_e32 v80, 0x3e16c740, v68
	v_ashrrev_i32_e32 v68, 31, v76
	v_lshrrev_b32_e32 v68, 19, v68
	v_add_u32_e32 v68, v76, v68
	v_and_b32_e32 v68, 0xffffe000, v68
	v_sub_u32_e32 v68, v76, v68
	v_ashrrev_i32_e32 v69, 31, v68
	v_lshlrev_b64 v[68:69], 7, v[68:69]
	v_lshl_add_u64 v[68:69], s[46:47], 0, v[68:69]
	v_lshl_add_u64 v[72:73], v[68:69], 0, v[30:31]
	s_waitcnt vmcnt(12)
; __device__ __forceinline__ unsigned cvt_pk_bf16(float lo, float hi) { f32x2 v = {lo, hi}; bf16x2_t b = __builtin_convertvector(v, bf16x2_t); return __builtin_bit_cast(unsigned, b); }
;     __device__ __forceinline__ void operator()(const f32x4 (&acc)[2][2][4][2], const u32x2 (&pf)[8], const g8::Unit& u, int wr, int wc, int fr, int fq) const {
;     ...
;                 if (u.pn == 1) {
;                     const float rq = __builtin_amdgcn_rsqf(sq.x * (1.f / 256.f) + 1e-6f) * SCALE_A;
;                     const float* cp = cs + ((size_t)(row % S) * 16 + 4 * fq) * 2;
;                     const f32x4 c0 = *(const f32x4*)cp, c1 = *(const f32x4*)(cp + 4);
;                     const float cc[4] = {c0[0], c0[2], c1[0], c1[2]}, sn[4] = {c0[1], c0[3], c1[1], c1[3]};
;                     {   const f32x4 t1 = acc[ai][0][m][0] * rq, t2 = acc[ai][0][m][1] * rq;
;                         float o1[4], o2[4];
; #pragma unroll
;                         for (int j = 0; j < 4; ++j) { o1[j] = t1[j] * cc[j] - t2[j] * sn[j]; o2[j] = t1[j] * sn[j] + t2[j] * cc[j]; }
;                         bf16_t* qp = QA + (size_t)row * 384 + wc * 96 + 64 + 4 * fq;
;                         *(u32x2*)qp = (u32x2){cvt_pk_bf16(o1[0], o1[1]), cvt_pk_bf16(o1[2], o1[3])};
;                         *(u32x2*)(qp + 16) = (u32x2){cvt_pk_bf16(o2[0], o2[1]), cvt_pk_bf16(o2[2], o2[3])}; }
;                     {   const bf16_t* hp = H + (size_t)row * HP + C_KR + 4 * fq;
;                         const u32x2 a = *(const u32x2*)hp, b = *(const u32x2*)(hp + 16);
;                         const float t1[4] = {__uint_as_float(a.x << 16), __uint_as_float(a.x & 0xffff0000u), __uint_as_float(a.y << 16), __uint_as_float(a.y & 0xffff0000u)};
;                         const float t2[4] = {__uint_as_float(b.x << 16), __uint_as_float(b.x & 0xffff0000u), __uint_as_float(b.y << 16), __uint_as_float(b.y & 0xffff0000u)};
;                         float o1[4], o2[4];
; #pragma unroll
;                         for (int j = 0; j < 4; ++j) { o1[j] = t1[j] * cc[j] - t2[j] * sn[j]; o2[j] = t1[j] * sn[j] + t2[j] * cc[j]; }
;                         bf16_t* kp = KA + (size_t)row * 384 + wc * 96 + 64 + 4 * fq;
;                         *(u32x2*)kp = (u32x2){cvt_pk_bf16(o1[0], o1[1]), cvt_pk_bf16(o1[2], o1[3])};
;                         *(u32x2*)(kp + 16) = (u32x2){cvt_pk_bf16(o2[0], o2[1]), cvt_pk_bf16(o2[2], o2[3])}; }
	ds_bpermute_b32 v206, v141, v206
	ds_bpermute_b32 v207, v141, v207
	ds_bpermute_b32 v208, v141, v208
	ds_bpermute_b32 v209, v141, v209
	ds_bpermute_b32 v210, v141, v210
	ds_bpermute_b32 v211, v141, v211
	ds_bpermute_b32 v212, v141, v212
	ds_bpermute_b32 v213, v141, v213
	ds_bpermute_b32 v214, v141, v214
	ds_bpermute_b32 v215, v141, v215
	ds_bpermute_b32 v216, v141, v216
	ds_bpermute_b32 v217, v141, v217
	s_waitcnt lgkmcnt(0)
	v_mov_b64_e32 v[68:69], v[206:207]
	v_mov_b64_e32 v[70:71], v[208:209]
	v_mov_b64_e32 v[72:73], v[210:211]
	v_mov_b64_e32 v[74:75], v[212:213]
	v_pk_mul_f32 v[84:85], v[80:81], v[60:61] op_sel_hi:[0,1]
	v_pk_mul_f32 v[82:83], v[80:81], v[64:65] op_sel_hi:[0,1]
	v_mov_b32_e32 v78, v73
	v_mov_b32_e32 v73, v74
	v_mov_b32_e32 v79, v75
	v_pk_mul_f32 v[74:75], v[84:85], v[72:73]
	s_nop 0
	v_pk_fma_f32 v[86:87], v[82:83], v[78:79], v[74:75]
	v_pk_mul_f32 v[74:75], v[84:85], v[78:79]
	v_pk_mul_f32 v[84:85], v[80:81], v[66:67] op_sel_hi:[0,1]
	v_pk_fma_f32 v[82:83], v[82:83], v[72:73], v[74:75] neg_lo:[0,0,1] neg_hi:[0,0,1]
	v_pk_mul_f32 v[80:81], v[80:81], v[62:63] op_sel_hi:[0,1]
	v_mov_b32_e32 v74, v69
	v_mov_b32_e32 v75, v71
	v_mov_b32_e32 v69, v70
	v_pk_mul_f32 v[70:71], v[80:81], v[68:69]
	v_pk_mul_f32 v[80:81], v[80:81], v[74:75]
	v_pk_fma_f32 v[70:71], v[84:85], v[74:75], v[70:71]
	v_pk_fma_f32 v[80:81], v[84:85], v[68:69], v[80:81] neg_lo:[0,0,1] neg_hi:[0,0,1]
	v_mov_b64_e32 v[84:85], s[54:55]
	v_mad_i64_i32 v[84:85], s[14:15], v76, s0, v[84:85]
	v_cvt_pk_bf16_f32 v82, v82, v83
	v_cvt_pk_bf16_f32 v83, v80, v81
	v_cvt_pk_bf16_f32 v81, v70, v71
	v_mov_b64_e32 v[70:71], s[44:45]
	v_lshl_add_u64 v[84:85], v[84:85], 0, v[88:89]
	v_cvt_pk_bf16_f32 v80, v86, v87
	v_mad_i64_i32 v[70:71], s[14:15], v76, s33, v[70:71]
	ds_bpermute_b32 v82, v140, v82
	ds_bpermute_b32 v83, v140, v83
	ds_bpermute_b32 v80, v140, v80
	ds_bpermute_b32 v81, v140, v81
	v_lshl_add_u64 v[156:157], v[144:145], 0, v[84:85]
	s_waitcnt lgkmcnt(0)
	global_store_dwordx2 v[156:157], v[82:83], off offset:128
	global_store_dwordx2 v[156:157], v[80:81], off offset:160
	v_lshl_add_u64 v[70:71], v[70:71], 0, v[88:89]
	s_waitcnt vmcnt(14)
	v_mov_b64_e32 v[80:81], v[214:215]
	v_mov_b64_e32 v[70:71], v[216:217]
	v_lshlrev_b32_e32 v82, 16, v80
	v_lshlrev_b32_e32 v84, 16, v70
	v_and_b32_e32 v85, 0xffff0000, v70
	v_and_b32_e32 v83, 0xffff0000, v80
	v_pk_mul_f32 v[86:87], v[72:73], v[84:85]
	v_lshlrev_b32_e32 v70, 16, v71
	v_pk_fma_f32 v[86:87], v[78:79], v[82:83], v[86:87]
	v_pk_mul_f32 v[78:79], v[78:79], v[84:85]
	v_and_b32_e32 v71, 0xffff0000, v71
	v_pk_fma_f32 v[72:73], v[72:73], v[82:83], v[78:79] neg_lo:[0,0,1] neg_hi:[0,0,1]
	v_lshlrev_b32_e32 v78, 16, v81
	v_and_b32_e32 v79, 0xffff0000, v81
	v_pk_mul_f32 v[80:81], v[68:69], v[70:71]
	v_pk_mul_f32 v[70:71], v[74:75], v[70:71]
	v_pk_fma_f32 v[80:81], v[74:75], v[78:79], v[80:81]
	v_pk_fma_f32 v[68:69], v[68:69], v[78:79], v[70:71] neg_lo:[0,0,1] neg_hi:[0,0,1]
	v_mov_b64_e32 v[70:71], s[56:57]
	v_mad_i64_i32 v[70:71], s[14:15], v76, s0, v[70:71]
	v_lshl_add_u64 v[70:71], v[70:71], 0, v[88:89]
	v_cvt_pk_bf16_f32 v72, v72, v73
	v_cvt_pk_bf16_f32 v73, v68, v69
	v_cvt_pk_bf16_f32 v68, v86, v87
	v_cvt_pk_bf16_f32 v69, v80, v81
	ds_bpermute_b32 v72, v140, v72
	ds_bpermute_b32 v73, v140, v73
	ds_bpermute_b32 v68, v140, v68
	ds_bpermute_b32 v69, v140, v69
	v_lshl_add_u64 v[156:157], v[144:145], 0, v[70:71]
	s_waitcnt lgkmcnt(0)
	global_store_dwordx2 v[156:157], v[72:73], off offset:128
	global_store_dwordx2 v[156:157], v[68:69], off offset:160
	s_mov_b64 s[14:15], 0

; __device__ __forceinline__ unsigned cvt_pk_bf16(float lo, float hi) { f32x2 v = {lo, hi}; bf16x2_t b = __builtin_convertvector(v, bf16x2_t); return __builtin_bit_cast(unsigned, b); }
;     __device__ __forceinline__ void operator()(const f32x4 (&acc)[2][2][4][2], const u32x2 (&pf)[8], const g8::Unit& u, int wr, int wc, int fr, int fq) const {
;     ...
;                 if (u.pn == 1) {
;                     const float rq = __builtin_amdgcn_rsqf(sq.x * (1.f / 256.f) + 1e-6f) * SCALE_A;
;                     const float* cp = cs + ((size_t)(row % S) * 16 + 4 * fq) * 2;
;                     const f32x4 c0 = *(const f32x4*)cp, c1 = *(const f32x4*)(cp + 4);
;                     const float cc[4] = {c0[0], c0[2], c1[0], c1[2]}, sn[4] = {c0[1], c0[3], c1[1], c1[3]};
;                     {   const f32x4 t1 = acc[ai][0][m][0] * rq, t2 = acc[ai][0][m][1] * rq;
;                         float o1[4], o2[4];
; #pragma unroll
;                         for (int j = 0; j < 4; ++j) { o1[j] = t1[j] * cc[j] - t2[j] * sn[j]; o2[j] = t1[j] * sn[j] + t2[j] * cc[j]; }
;                         bf16_t* qp = QA + (size_t)row * 384 + wc * 96 + 64 + 4 * fq;
;                         *(u32x2*)qp = (u32x2){cvt_pk_bf16(o1[0], o1[1]), cvt_pk_bf16(o1[2], o1[3])};
;                         *(u32x2*)(qp + 16) = (u32x2){cvt_pk_bf16(o2[0], o2[1]), cvt_pk_bf16(o2[2], o2[3])}; }
;                     {   const bf16_t* hp = H + (size_t)row * HP + C_KR + 4 * fq;
;                         const u32x2 a = *(const u32x2*)hp, b = *(const u32x2*)(hp + 16);
;                         const float t1[4] = {__uint_as_float(a.x << 16), __uint_as_float(a.x & 0xffff0000u), __uint_as_float(a.y << 16), __uint_as_float(a.y & 0xffff0000u)};
;                         const float t2[4] = {__uint_as_float(b.x << 16), __uint_as_float(b.x & 0xffff0000u), __uint_as_float(b.y << 16), __uint_as_float(b.y & 0xffff0000u)};
;                         float o1[4], o2[4];
; #pragma unroll
;                         for (int j = 0; j < 4; ++j) { o1[j] = t1[j] * cc[j] - t2[j] * sn[j]; o2[j] = t1[j] * sn[j] + t2[j] * cc[j]; }
;                         bf16_t* kp = KA + (size_t)row * 384 + wc * 96 + 64 + 4 * fq;
;                         *(u32x2*)kp = (u32x2){cvt_pk_bf16(o1[0], o1[1]), cvt_pk_bf16(o1[2], o1[3])};
;                         *(u32x2*)(kp + 16) = (u32x2){cvt_pk_bf16(o2[0], o2[1]), cvt_pk_bf16(o2[2], o2[3])}; }
.LBB0_676:
	s_cmp_eq_u32 s67, 1
	s_mov_b64 s[14:15], -1
	s_cbranch_scc0 .LBB0_678
	v_fmamk_f32 v52, v166, 0x3b800000, v246
	v_rsq_f32_e32 v52, v52
	v_lshlrev_b32_e32 v72, 1, v5
	v_mov_b32_e32 v73, v31
	v_mul_f32_e32 v64, 0x3e16c740, v52
	v_ashrrev_i32_e32 v52, 31, v60
	v_lshrrev_b32_e32 v52, 19, v52
	v_add_u32_e32 v52, v60, v52
	v_and_b32_e32 v52, 0xffffe000, v52
	v_sub_u32_e32 v52, v60, v52
	v_ashrrev_i32_e32 v53, 31, v52
	v_lshlrev_b64 v[52:53], 7, v[52:53]
	v_lshl_add_u64 v[52:53], s[46:47], 0, v[52:53]
	v_lshl_add_u64 v[56:57], v[52:53], 0, v[30:31]
	s_waitcnt vmcnt(12)
	ds_bpermute_b32 v218, v141, v218
	ds_bpermute_b32 v219, v141, v219
	ds_bpermute_b32 v220, v141, v220
	ds_bpermute_b32 v221, v141, v221
	ds_bpermute_b32 v222, v141, v222
	ds_bpermute_b32 v223, v141, v223
	ds_bpermute_b32 v224, v141, v224
	ds_bpermute_b32 v225, v141, v225
	ds_bpermute_b32 v226, v141, v226
	ds_bpermute_b32 v227, v141, v227
	ds_bpermute_b32 v228, v141, v228
	ds_bpermute_b32 v229, v141, v229
	s_waitcnt lgkmcnt(0)
	v_mov_b64_e32 v[52:53], v[218:219]
	v_mov_b64_e32 v[54:55], v[220:221]
	v_mov_b64_e32 v[56:57], v[222:223]
	v_mov_b64_e32 v[58:59], v[224:225]
	v_pk_mul_f32 v[68:69], v[64:65], v[44:45] op_sel_hi:[0,1]
	v_pk_mul_f32 v[66:67], v[64:65], v[48:49] op_sel_hi:[0,1]
	v_mov_b32_e32 v62, v57
	v_mov_b32_e32 v57, v58
	v_mov_b32_e32 v63, v59
	v_pk_mul_f32 v[58:59], v[68:69], v[56:57]
	s_nop 0
	v_pk_fma_f32 v[70:71], v[66:67], v[62:63], v[58:59]
	v_pk_mul_f32 v[58:59], v[68:69], v[62:63]
	v_pk_mul_f32 v[68:69], v[64:65], v[50:51] op_sel_hi:[0,1]
	v_pk_fma_f32 v[66:67], v[66:67], v[56:57], v[58:59] neg_lo:[0,0,1] neg_hi:[0,0,1]
	v_pk_mul_f32 v[64:65], v[64:65], v[46:47] op_sel_hi:[0,1]
	v_mov_b32_e32 v58, v53
	v_mov_b32_e32 v59, v55
	v_mov_b32_e32 v53, v54
	v_pk_mul_f32 v[54:55], v[64:65], v[52:53]
	v_pk_mul_f32 v[64:65], v[64:65], v[58:59]
	v_pk_fma_f32 v[54:55], v[68:69], v[58:59], v[54:55]
	v_pk_fma_f32 v[64:65], v[68:69], v[52:53], v[64:65] neg_lo:[0,0,1] neg_hi:[0,0,1]
	v_mov_b64_e32 v[68:69], s[54:55]
	v_mad_i64_i32 v[68:69], s[14:15], v60, s0, v[68:69]
	v_cvt_pk_bf16_f32 v66, v66, v67
	v_cvt_pk_bf16_f32 v67, v64, v65
	v_cvt_pk_bf16_f32 v65, v54, v55
	v_mov_b64_e32 v[54:55], s[44:45]
	v_lshl_add_u64 v[68:69], v[68:69], 0, v[72:73]
	v_cvt_pk_bf16_f32 v64, v70, v71
	v_mad_i64_i32 v[54:55], s[14:15], v60, s33, v[54:55]
	ds_bpermute_b32 v66, v140, v66
	ds_bpermute_b32 v67, v140, v67
	ds_bpermute_b32 v64, v140, v64
	ds_bpermute_b32 v65, v140, v65
	v_lshl_add_u64 v[156:157], v[144:145], 0, v[68:69]
	s_waitcnt lgkmcnt(0)
	global_store_dwordx2 v[156:157], v[66:67], off offset:128
	global_store_dwordx2 v[156:157], v[64:65], off offset:160
	v_lshl_add_u64 v[54:55], v[54:55], 0, v[72:73]
	s_waitcnt vmcnt(14)
	v_mov_b64_e32 v[64:65], v[226:227]
	v_mov_b64_e32 v[54:55], v[228:229]
	v_lshlrev_b32_e32 v66, 16, v64
	v_lshlrev_b32_e32 v68, 16, v54
	v_and_b32_e32 v69, 0xffff0000, v54
	v_and_b32_e32 v67, 0xffff0000, v64
	v_pk_mul_f32 v[70:71], v[56:57], v[68:69]
	v_lshlrev_b32_e32 v54, 16, v55
	v_pk_fma_f32 v[70:71], v[62:63], v[66:67], v[70:71]
	v_pk_mul_f32 v[62:63], v[62:63], v[68:69]
	v_and_b32_e32 v55, 0xffff0000, v55
	v_pk_fma_f32 v[56:57], v[56:57], v[66:67], v[62:63] neg_lo:[0,0,1] neg_hi:[0,0,1]
	v_lshlrev_b32_e32 v62, 16, v65
	v_and_b32_e32 v63, 0xffff0000, v65
	v_pk_mul_f32 v[64:65], v[52:53], v[54:55]
	v_pk_mul_f32 v[54:55], v[58:59], v[54:55]
	v_pk_fma_f32 v[64:65], v[58:59], v[62:63], v[64:65]
	v_pk_fma_f32 v[52:53], v[52:53], v[62:63], v[54:55] neg_lo:[0,0,1] neg_hi:[0,0,1]
	v_mov_b64_e32 v[54:55], s[56:57]
	v_mad_i64_i32 v[54:55], s[14:15], v60, s0, v[54:55]
	v_lshl_add_u64 v[54:55], v[54:55], 0, v[72:73]
	v_cvt_pk_bf16_f32 v56, v56, v57
	v_cvt_pk_bf16_f32 v57, v52, v53
	v_cvt_pk_bf16_f32 v52, v70, v71
	v_cvt_pk_bf16_f32 v53, v64, v65
	ds_bpermute_b32 v56, v140, v56
	ds_bpermute_b32 v57, v140, v57
	ds_bpermute_b32 v52, v140, v52
	ds_bpermute_b32 v53, v140, v53
	v_lshl_add_u64 v[156:157], v[144:145], 0, v[54:55]
	s_waitcnt lgkmcnt(0)
	global_store_dwordx2 v[156:157], v[56:57], off offset:128
	global_store_dwordx2 v[156:157], v[52:53], off offset:160
	s_mov_b64 s[14:15], 0

; __device__ __forceinline__ unsigned cvt_pk_bf16(float lo, float hi) { f32x2 v = {lo, hi}; bf16x2_t b = __builtin_convertvector(v, bf16x2_t); return __builtin_bit_cast(unsigned, b); }
;     __device__ __forceinline__ void operator()(const f32x4 (&acc)[2][2][4][2], const u32x2 (&pf)[8], const g8::Unit& u, int wr, int wc, int fr, int fq) const {
;     ...
;                 if (u.pn == 1) {
;                     const float rq = __builtin_amdgcn_rsqf(sq.x * (1.f / 256.f) + 1e-6f) * SCALE_A;
;                     const float* cp = cs + ((size_t)(row % S) * 16 + 4 * fq) * 2;
;                     const f32x4 c0 = *(const f32x4*)cp, c1 = *(const f32x4*)(cp + 4);
;                     const float cc[4] = {c0[0], c0[2], c1[0], c1[2]}, sn[4] = {c0[1], c0[3], c1[1], c1[3]};
;                     {   const f32x4 t1 = acc[ai][0][m][0] * rq, t2 = acc[ai][0][m][1] * rq;
;                         float o1[4], o2[4];
; #pragma unroll
;                         for (int j = 0; j < 4; ++j) { o1[j] = t1[j] * cc[j] - t2[j] * sn[j]; o2[j] = t1[j] * sn[j] + t2[j] * cc[j]; }
;                         bf16_t* qp = QA + (size_t)row * 384 + wc * 96 + 64 + 4 * fq;
;                         *(u32x2*)qp = (u32x2){cvt_pk_bf16(o1[0], o1[1]), cvt_pk_bf16(o1[2], o1[3])};
;                         *(u32x2*)(qp + 16) = (u32x2){cvt_pk_bf16(o2[0], o2[1]), cvt_pk_bf16(o2[2], o2[3])}; }
;                     {   const bf16_t* hp = H + (size_t)row * HP + C_KR + 4 * fq;
;                         const u32x2 a = *(const u32x2*)hp, b = *(const u32x2*)(hp + 16);
;                         const float t1[4] = {__uint_as_float(a.x << 16), __uint_as_float(a.x & 0xffff0000u), __uint_as_float(a.y << 16), __uint_as_float(a.y & 0xffff0000u)};
;                         const float t2[4] = {__uint_as_float(b.x << 16), __uint_as_float(b.x & 0xffff0000u), __uint_as_float(b.y << 16), __uint_as_float(b.y & 0xffff0000u)};
;                         float o1[4], o2[4];
; #pragma unroll
;                         for (int j = 0; j < 4; ++j) { o1[j] = t1[j] * cc[j] - t2[j] * sn[j]; o2[j] = t1[j] * sn[j] + t2[j] * cc[j]; }
;                         bf16_t* kp = KA + (size_t)row * 384 + wc * 96 + 64 + 4 * fq;
;                         *(u32x2*)kp = (u32x2){cvt_pk_bf16(o1[0], o1[1]), cvt_pk_bf16(o1[2], o1[3])};
;                         *(u32x2*)(kp + 16) = (u32x2){cvt_pk_bf16(o2[0], o2[1]), cvt_pk_bf16(o2[2], o2[3])}; }
.LBB0_703:
	s_cmp_eq_u32 s67, 1
	s_mov_b64 s[14:15], -1
	s_cbranch_scc0 .LBB0_705
	v_fmamk_f32 v36, v162, 0x3b800000, v246
	v_rsq_f32_e32 v36, v36
	v_lshlrev_b32_e32 v56, 1, v5
	v_mov_b32_e32 v57, v31
	v_mul_f32_e32 v48, 0x3e16c740, v36
	v_ashrrev_i32_e32 v36, 31, v44
	v_lshrrev_b32_e32 v36, 19, v36
	v_add_u32_e32 v36, v44, v36
	v_and_b32_e32 v36, 0xffffe000, v36
	v_sub_u32_e32 v36, v44, v36
	v_ashrrev_i32_e32 v37, 31, v36
	v_lshlrev_b64 v[36:37], 7, v[36:37]
	v_lshl_add_u64 v[36:37], s[46:47], 0, v[36:37]
	v_lshl_add_u64 v[40:41], v[36:37], 0, v[30:31]
	s_waitcnt vmcnt(12)
	ds_bpermute_b32 v230, v141, v230
	ds_bpermute_b32 v231, v141, v231
	ds_bpermute_b32 v232, v141, v232
	ds_bpermute_b32 v233, v141, v233
	ds_bpermute_b32 v234, v141, v234
	ds_bpermute_b32 v235, v141, v235
	ds_bpermute_b32 v236, v141, v236
	ds_bpermute_b32 v237, v141, v237
	ds_bpermute_b32 v238, v141, v238
	ds_bpermute_b32 v239, v141, v239
	ds_bpermute_b32 v240, v141, v240
	ds_bpermute_b32 v241, v141, v241
	s_waitcnt lgkmcnt(0)
	v_mov_b64_e32 v[36:37], v[230:231]
	v_mov_b64_e32 v[38:39], v[232:233]
	v_mov_b64_e32 v[40:41], v[234:235]
	v_mov_b64_e32 v[42:43], v[236:237]
	v_pk_mul_f32 v[52:53], v[48:49], v[26:27] op_sel_hi:[0,1]
	v_pk_mul_f32 v[50:51], v[48:49], v[32:33] op_sel_hi:[0,1]
	v_mov_b32_e32 v46, v41
	v_mov_b32_e32 v41, v42
	v_mov_b32_e32 v47, v43
	v_pk_mul_f32 v[42:43], v[52:53], v[40:41]
	s_nop 0
	v_pk_fma_f32 v[54:55], v[50:51], v[46:47], v[42:43]
	v_pk_mul_f32 v[42:43], v[52:53], v[46:47]
	v_pk_mul_f32 v[52:53], v[48:49], v[34:35] op_sel_hi:[0,1]
	v_pk_fma_f32 v[50:51], v[50:51], v[40:41], v[42:43] neg_lo:[0,0,1] neg_hi:[0,0,1]
	v_pk_mul_f32 v[48:49], v[48:49], v[28:29] op_sel_hi:[0,1]
	v_mov_b32_e32 v42, v37
	v_mov_b32_e32 v43, v39
	v_mov_b32_e32 v37, v38
	v_pk_mul_f32 v[38:39], v[48:49], v[36:37]
	v_pk_mul_f32 v[48:49], v[48:49], v[42:43]
	v_pk_fma_f32 v[38:39], v[52:53], v[42:43], v[38:39]
	v_pk_fma_f32 v[48:49], v[52:53], v[36:37], v[48:49] neg_lo:[0,0,1] neg_hi:[0,0,1]
	v_mov_b64_e32 v[52:53], s[54:55]
	v_mad_i64_i32 v[52:53], s[14:15], v44, s0, v[52:53]
	v_cvt_pk_bf16_f32 v50, v50, v51
	v_cvt_pk_bf16_f32 v51, v48, v49
	v_cvt_pk_bf16_f32 v49, v38, v39
	v_mov_b64_e32 v[38:39], s[44:45]
	v_lshl_add_u64 v[52:53], v[52:53], 0, v[56:57]
	v_cvt_pk_bf16_f32 v48, v54, v55
	v_mad_i64_i32 v[38:39], s[14:15], v44, s33, v[38:39]
	ds_bpermute_b32 v50, v140, v50
	ds_bpermute_b32 v51, v140, v51
	ds_bpermute_b32 v48, v140, v48
	ds_bpermute_b32 v49, v140, v49
	v_lshl_add_u64 v[156:157], v[144:145], 0, v[52:53]
	s_waitcnt lgkmcnt(0)
	global_store_dwordx2 v[156:157], v[50:51], off offset:128
	global_store_dwordx2 v[156:157], v[48:49], off offset:160
	v_lshl_add_u64 v[38:39], v[38:39], 0, v[56:57]
	s_waitcnt vmcnt(14)
	v_mov_b64_e32 v[48:49], v[238:239]
	v_mov_b64_e32 v[38:39], v[240:241]
	v_lshlrev_b32_e32 v50, 16, v48
	v_lshlrev_b32_e32 v52, 16, v38
	v_and_b32_e32 v53, 0xffff0000, v38
	v_and_b32_e32 v51, 0xffff0000, v48
	v_pk_mul_f32 v[54:55], v[40:41], v[52:53]
	v_lshlrev_b32_e32 v38, 16, v39
	v_pk_fma_f32 v[54:55], v[46:47], v[50:51], v[54:55]
	v_pk_mul_f32 v[46:47], v[46:47], v[52:53]
	v_and_b32_e32 v39, 0xffff0000, v39
	v_pk_fma_f32 v[40:41], v[40:41], v[50:51], v[46:47] neg_lo:[0,0,1] neg_hi:[0,0,1]
	v_lshlrev_b32_e32 v46, 16, v49
	v_and_b32_e32 v47, 0xffff0000, v49
	v_pk_mul_f32 v[48:49], v[36:37], v[38:39]
	v_pk_mul_f32 v[38:39], v[42:43], v[38:39]
	v_pk_fma_f32 v[48:49], v[42:43], v[46:47], v[48:49]
	v_pk_fma_f32 v[36:37], v[36:37], v[46:47], v[38:39] neg_lo:[0,0,1] neg_hi:[0,0,1]
	v_mov_b64_e32 v[38:39], s[56:57]
	v_mad_i64_i32 v[38:39], s[14:15], v44, s0, v[38:39]
	v_lshl_add_u64 v[38:39], v[38:39], 0, v[56:57]
	v_cvt_pk_bf16_f32 v40, v40, v41
	v_cvt_pk_bf16_f32 v41, v36, v37
	v_cvt_pk_bf16_f32 v36, v54, v55
	v_cvt_pk_bf16_f32 v37, v48, v49
	ds_bpermute_b32 v40, v140, v40
	ds_bpermute_b32 v41, v140, v41
	ds_bpermute_b32 v36, v140, v36
	ds_bpermute_b32 v37, v140, v37
	v_lshl_add_u64 v[156:157], v[144:145], 0, v[38:39]
	s_waitcnt lgkmcnt(0)
	global_store_dwordx2 v[156:157], v[40:41], off offset:128
	global_store_dwordx2 v[156:157], v[36:37], off offset:160
	s_mov_b64 s[14:15], 0

; __device__ __forceinline__ unsigned cvt_pk_bf16(float lo, float hi) { f32x2 v = {lo, hi}; bf16x2_t b = __builtin_convertvector(v, bf16x2_t); return __builtin_bit_cast(unsigned, b); }
;     __device__ __forceinline__ void operator()(const f32x4 (&acc)[2][2][4][2], const u32x2 (&pf)[8], const g8::Unit& u, int wr, int wc, int fr, int fq) const {
;     ...
;                 if (u.pn == 1) {
;                     const float rq = __builtin_amdgcn_rsqf(sq.x * (1.f / 256.f) + 1e-6f) * SCALE_A;
;                     const float* cp = cs + ((size_t)(row % S) * 16 + 4 * fq) * 2;
;                     const f32x4 c0 = *(const f32x4*)cp, c1 = *(const f32x4*)(cp + 4);
;                     const float cc[4] = {c0[0], c0[2], c1[0], c1[2]}, sn[4] = {c0[1], c0[3], c1[1], c1[3]};
;                     {   const f32x4 t1 = acc[ai][0][m][0] * rq, t2 = acc[ai][0][m][1] * rq;
;                         float o1[4], o2[4];
; #pragma unroll
;                         for (int j = 0; j < 4; ++j) { o1[j] = t1[j] * cc[j] - t2[j] * sn[j]; o2[j] = t1[j] * sn[j] + t2[j] * cc[j]; }
;                         bf16_t* qp = QA + (size_t)row * 384 + wc * 96 + 64 + 4 * fq;
;                         *(u32x2*)qp = (u32x2){cvt_pk_bf16(o1[0], o1[1]), cvt_pk_bf16(o1[2], o1[3])};
;                         *(u32x2*)(qp + 16) = (u32x2){cvt_pk_bf16(o2[0], o2[1]), cvt_pk_bf16(o2[2], o2[3])}; }
;                     {   const bf16_t* hp = H + (size_t)row * HP + C_KR + 4 * fq;
;                         const u32x2 a = *(const u32x2*)hp, b = *(const u32x2*)(hp + 16);
;                         const float t1[4] = {__uint_as_float(a.x << 16), __uint_as_float(a.x & 0xffff0000u), __uint_as_float(a.y << 16), __uint_as_float(a.y & 0xffff0000u)};
;                         const float t2[4] = {__uint_as_float(b.x << 16), __uint_as_float(b.x & 0xffff0000u), __uint_as_float(b.y << 16), __uint_as_float(b.y & 0xffff0000u)};
;                         float o1[4], o2[4];
; #pragma unroll
;                         for (int j = 0; j < 4; ++j) { o1[j] = t1[j] * cc[j] - t2[j] * sn[j]; o2[j] = t1[j] * sn[j] + t2[j] * cc[j]; }
;                         bf16_t* kp = KA + (size_t)row * 384 + wc * 96 + 64 + 4 * fq;
;                         *(u32x2*)kp = (u32x2){cvt_pk_bf16(o1[0], o1[1]), cvt_pk_bf16(o1[2], o1[3])};
;                         *(u32x2*)(kp + 16) = (u32x2){cvt_pk_bf16(o2[0], o2[1]), cvt_pk_bf16(o2[2], o2[3])}; }
.LBB0_730:
	s_cmp_eq_u32 s67, 1
	s_mov_b64 s[14:15], -1
	s_cbranch_scc0 .LBB0_732
	v_fmamk_f32 v18, v160, 0x3b800000, v246
	v_rsq_f32_e32 v18, v18
	v_lshlrev_b32_e32 v40, 1, v5
	v_mov_b32_e32 v41, v31
	v_mul_f32_e32 v32, 0x3e16c740, v18
	v_ashrrev_i32_e32 v18, 31, v26
	v_lshrrev_b32_e32 v18, 19, v18
	v_add_u32_e32 v18, v26, v18
	v_and_b32_e32 v18, 0xffffe000, v18
	v_sub_u32_e32 v18, v26, v18
	v_ashrrev_i32_e32 v19, 31, v18
	v_lshlrev_b64 v[18:19], 7, v[18:19]
	v_lshl_add_u64 v[18:19], s[46:47], 0, v[18:19]
	v_lshl_add_u64 v[22:23], v[18:19], 0, v[30:31]
	s_waitcnt vmcnt(12)
	ds_bpermute_b32 v242, v141, v242
	ds_bpermute_b32 v243, v141, v243
	ds_bpermute_b32 v244, v141, v244
	ds_bpermute_b32 v245, v141, v245
	ds_bpermute_b32 v188, v141, v188
	ds_bpermute_b32 v189, v141, v189
	ds_bpermute_b32 v190, v141, v190
	ds_bpermute_b32 v191, v141, v191
	ds_bpermute_b32 v192, v141, v192
	ds_bpermute_b32 v193, v141, v193
	ds_bpermute_b32 v194, v141, v194
	ds_bpermute_b32 v195, v141, v195
	s_waitcnt lgkmcnt(0)
	v_mov_b64_e32 v[18:19], v[242:243]
	v_mov_b64_e32 v[20:21], v[244:245]
	v_mov_b64_e32 v[22:23], v[188:189]
	v_mov_b64_e32 v[24:25], v[190:191]
	v_pk_mul_f32 v[36:37], v[32:33], v[10:11] op_sel_hi:[0,1]
	v_pk_mul_f32 v[34:35], v[32:33], v[14:15] op_sel_hi:[0,1]
	v_mov_b32_e32 v28, v23
	v_mov_b32_e32 v23, v24
	v_mov_b32_e32 v29, v25
	v_pk_mul_f32 v[24:25], v[36:37], v[22:23]
	s_nop 0
	v_pk_fma_f32 v[38:39], v[34:35], v[28:29], v[24:25]
	v_pk_mul_f32 v[24:25], v[36:37], v[28:29]
	v_pk_mul_f32 v[36:37], v[32:33], v[16:17] op_sel_hi:[0,1]
	v_pk_fma_f32 v[34:35], v[34:35], v[22:23], v[24:25] neg_lo:[0,0,1] neg_hi:[0,0,1]
	v_pk_mul_f32 v[32:33], v[32:33], v[12:13] op_sel_hi:[0,1]
	v_mov_b32_e32 v24, v19
	v_mov_b32_e32 v25, v21
	v_mov_b32_e32 v19, v20
	v_pk_mul_f32 v[20:21], v[32:33], v[18:19]
	v_pk_mul_f32 v[32:33], v[32:33], v[24:25]
	v_pk_fma_f32 v[20:21], v[36:37], v[24:25], v[20:21]
	v_pk_fma_f32 v[32:33], v[36:37], v[18:19], v[32:33] neg_lo:[0,0,1] neg_hi:[0,0,1]
	v_mov_b64_e32 v[36:37], s[54:55]
	v_mad_i64_i32 v[36:37], s[14:15], v26, s0, v[36:37]
	v_cvt_pk_bf16_f32 v34, v34, v35
	v_cvt_pk_bf16_f32 v35, v32, v33
	v_cvt_pk_bf16_f32 v33, v20, v21
	v_mov_b64_e32 v[20:21], s[44:45]
	v_lshl_add_u64 v[36:37], v[36:37], 0, v[40:41]
	v_cvt_pk_bf16_f32 v32, v38, v39
	v_mad_i64_i32 v[20:21], s[14:15], v26, s33, v[20:21]
	ds_bpermute_b32 v34, v140, v34
	ds_bpermute_b32 v35, v140, v35
	ds_bpermute_b32 v32, v140, v32
	ds_bpermute_b32 v33, v140, v33
	v_lshl_add_u64 v[156:157], v[144:145], 0, v[36:37]
	s_waitcnt lgkmcnt(0)
	global_store_dwordx2 v[156:157], v[34:35], off offset:128
	global_store_dwordx2 v[156:157], v[32:33], off offset:160
	v_lshl_add_u64 v[20:21], v[20:21], 0, v[40:41]
	s_waitcnt vmcnt(14)
	v_mov_b64_e32 v[32:33], v[192:193]
	v_mov_b64_e32 v[20:21], v[194:195]
	v_lshlrev_b32_e32 v34, 16, v32
	v_lshlrev_b32_e32 v36, 16, v20
	v_and_b32_e32 v37, 0xffff0000, v20
	v_and_b32_e32 v35, 0xffff0000, v32
	v_pk_mul_f32 v[38:39], v[22:23], v[36:37]
	v_lshlrev_b32_e32 v20, 16, v21
	v_pk_fma_f32 v[38:39], v[28:29], v[34:35], v[38:39]
	v_pk_mul_f32 v[28:29], v[28:29], v[36:37]
	v_and_b32_e32 v21, 0xffff0000, v21
	v_pk_fma_f32 v[22:23], v[22:23], v[34:35], v[28:29] neg_lo:[0,0,1] neg_hi:[0,0,1]
	v_lshlrev_b32_e32 v28, 16, v33
	v_and_b32_e32 v29, 0xffff0000, v33
	v_pk_mul_f32 v[32:33], v[18:19], v[20:21]
	v_pk_mul_f32 v[20:21], v[24:25], v[20:21]
	v_pk_fma_f32 v[32:33], v[24:25], v[28:29], v[32:33]
	v_pk_fma_f32 v[18:19], v[18:19], v[28:29], v[20:21] neg_lo:[0,0,1] neg_hi:[0,0,1]
	v_mov_b64_e32 v[20:21], s[56:57]
	v_mad_i64_i32 v[20:21], s[14:15], v26, s0, v[20:21]
	v_lshl_add_u64 v[20:21], v[20:21], 0, v[40:41]
	v_cvt_pk_bf16_f32 v22, v22, v23
	v_cvt_pk_bf16_f32 v23, v18, v19
	v_cvt_pk_bf16_f32 v18, v38, v39
	v_cvt_pk_bf16_f32 v19, v32, v33
	ds_bpermute_b32 v22, v140, v22
	ds_bpermute_b32 v23, v140, v23
	ds_bpermute_b32 v18, v140, v18
	ds_bpermute_b32 v19, v140, v19
	v_lshl_add_u64 v[156:157], v[144:145], 0, v[20:21]
	s_waitcnt lgkmcnt(0)
	global_store_dwordx2 v[156:157], v[22:23], off offset:128
	global_store_dwordx2 v[156:157], v[18:19], off offset:160
	s_mov_b64 s[14:15], 0
